# split of the 24 conversion units per wave: 12 in the attention loop, 6 in the top-k loop, 6 left in phase 2
# speedup vs baseline: 1.0075x; 1.0075x over previous
; #define LAS __attribute__((address_space(3)))
; __device__ __forceinline__ void convert_experts(Frame& F, int lo, int hi) {
;     const int gw = F.vcu * 8 + F.wave, NGW = F.G * 8;
;     LAS unsigned char* scr = F.lds + F.wave * 16384;
;     unsigned char* W1t = WSP(F, WS_W1T, unsigned char); unsigned char* W2t = WSP(F, WS_W2T, unsigned char);
;     const float* weg = F.a->in[I_WEG]; const float* weu = F.a->in[I_WEU]; const float* wed = F.a->in[I_WED];
;     const float* wsg = F.a->in[I_WSG]; const float* wsu = F.a->in[I_WSU]; const float* wsd = F.a->in[I_WSD];
;     ...
;     constexpr int NPAIRS = CONV_ITEMS / 2;
;     (void)lo; (void)hi;
;     ...
;     if (gw < NPAIRS) {
;         const int ns = 2 * ((NPAIRS - gw + NGW - 1) / NGW);
;         int sq = 0, r = CONV_RIDX(0);
;         TItem tc, tn; CONV_DESC(r, tc); tn = tc;
.Lcv1_vcu:
	s_lshl_b32 s11, s11, 3
	s_add_u32 s89, s11, s9
	s_lshl_b32 s71, s8, 3
	s_mul_i32 s10, s71, 18
	s_add_u32 s89, s89, s10
	s_mov_b32 s69, s89
	s_add_u32 s86, s84, 0x9180000
	s_addc_u32 s87, s85, 0
	s_add_u32 s84, s84, 0x1100000
	s_addc_u32 s85, s85, 0
	s_mov_b32 s90, 0xc2b8aa3b
	s_cmp_ge_u32 s89, 49344
	s_cbranch_scc1 .Lcv1_done
	s_cmp_lt_u32 s69, 49344
	s_cbranch_scc0 .Lcv1_dummyA1
	s_lshr_b32 s10, s69, 6
	s_and_b32 s12, s69, 63
	s_mul_hi_u32 s14, s10, 0xaaaaaaab
	s_lshr_b32 s14, s14, 1
	s_mul_i32 s11, s14, 3
	s_sub_u32 s11, s10, s11
	s_cmp_lt_u32 s14, 256
	s_cselect_b32 s10, s14, 0
	s_cselect_b64 s[44:45], -1, 0
	s_lshl_b32 s10, s10, 20
	s_cmp_eq_u32 s11, 2
	s_cbranch_scc1 .Lcv1_downA1
	s_cmp_eq_u32 s11, 0
	s_cselect_b64 s[4:5], s[72:73], s[74:75]
	s_cselect_b64 s[38:39], s[78:79], s[80:81]
	s_mov_b32 s94, 0xc3317218
	s_cselect_b32 s94, s90, s94
	s_cmp_lg_u64 s[44:45], 0
	s_cselect_b64 s[4:5], s[4:5], s[38:39]
	s_lshr_b32 s38, s12, 3
	s_and_b32 s39, s12, 7
	s_lshl_b32 s8, s38, 17
	s_add_u32 s10, s10, s8
	s_lshl_b32 s8, s39, 7
	s_add_u32 s10, s10, s8
	s_add_u32 s4, s4, s10
	s_addc_u32 s5, s5, 0
	s_lshl_b32 s14, s14, 19
	s_lshr_b32 s8, s39, 2
	s_lshl_b32 s8, s8, 18
	s_add_u32 s14, s14, s8
	s_and_b32 s8, s39, 3
	s_lshl_b32 s8, s8, 15
	s_add_u32 s14, s14, s8
	s_lshl_b32 s8, s11, 17
	s_add_u32 s14, s14, s8
	s_lshl_b32 s8, s38, 7
	s_add_u32 s14, s14, s8
	s_add_u32 s92, s84, s14
	s_addc_u32 s93, s85, 0
	s_movk_i32 s25, 0x400
	s_movk_i32 s27, 0x1000
	s_movk_i32 s8, 0x400
	s_movk_i32 s9, 0x4000
	s_branch .Lcv1_goA1

; #define LAS __attribute__((address_space(3)))
; __device__ __forceinline__ void router_topk(Frame& F, int tile) {
;     const float* logits = WSP(F, WS_B, float); const float* br = F.a->in[I_BR];
;     int* tk_e = WSP(F, WS_TOPK_E, int); float* tk_g = WSP(F, WS_TOPK_G, float); int* tk_p = WSP(F, WS_TOPK_P, int);
;     int* gcnt = (int*)(F.a->ws + WS_CTL + CTL_CNT);
;     LAS int* hist = (LAS int*)F.lds; LAS int* base = hist + 256;
;     const int lane = F.lane, w = F.wave;
;     if (F.tid < 256) hist[F.tid] = 0;
;     __syncthreads();
;     const f32x4 bias = *(const f32x4*)(br + 4 * lane);
;     f32x4 lgn = *(const f32x4*)(logits + (size_t)(tile * 256 + w * 32) * 256 + 4 * lane);
;     int pe = 0, pp = 0; float pg = 0.f;
;     int* dumpi = (int*)(F.a->ws + WS_B + ((size_t)128 << 20));
.Lcvt_vcu:
	s_add_u32 s69, s41, s40
	s_and_b32 s69, s69, 3
	s_lshl_b32 s41, s41, 3
	s_add_u32 s89, s41, s40
	s_lshl_b32 s71, s64, 3
	s_mul_i32 s39, s71, 12
	s_add_u32 s89, s89, s39
	s_movk_i32 s90, 6
	s_mov_b32 s32, 0
	s_add_u32 s86, s84, 0x9180000
	s_addc_u32 s87, s85, 0
	s_add_u32 s84, s84, 0x1100000
	s_addc_u32 s85, s85, 0
	s_add_u32 s14, s8, 0x900000
	s_addc_u32 s15, s9, 0
	s_add_u32 s16, s8, 0xb00000
	s_addc_u32 s17, s9, 0
	s_add_u32 s18, s8, 0xd00000
	s_addc_u32 s19, s9, 0
	v_mov_b32_e32 v131, 0
	s_add_u32 s20, s8, 0x4000
	v_mov_b32_e32 v133, v131
	s_addc_u32 s21, s9, 0
	v_lshl_add_u64 v[2:3], s[8:9], 0, v[132:133]
	s_mov_b64 s[8:9], 0x1d1c0000
	s_waitcnt vmcnt(0)
	v_lshl_add_u64 v[12:13], v[2:3], 0, s[8:9]
	s_mov_b64 s[8:9], 0x1d1c0100
	s_movk_i32 s4, 0x100
	v_mov_b32_e32 v135, v131
	v_lshl_add_u64 v[14:15], v[2:3], 0, s[8:9]
	s_mov_b64 s[8:9], 0x1d1c0200
	v_cmp_gt_i32_e64 s[4:5], s4, v1
	s_mov_b32 s26, 0
	v_lshl_add_u32 v22, v1, 2, 0
	s_lshl_b32 s27, s49, 5
	v_lshl_add_u64 v[10:11], s[6:7], 0, v[134:135]
	v_cmp_gt_u32_e64 s[6:7], 8, v130
	v_lshl_add_u64 v[16:17], v[2:3], 0, s[8:9]
	v_mov_b64_e32 v[18:19], 0x100
	v_mov_b64_e32 v[20:21], 0xff
	v_mov_b32_e32 v23, 0xff800000
	v_mov_b32_e32 v24, 1
	s_waitcnt vmcnt(0)
	s_barrier
	s_branch .LBB0_532
